# speedup vs baseline: 1.0008x; 1.0008x over previous
.LBB0_20:
	s_or_b64 exec, exec, s[0:1]
	v_lshrrev_b32_e32 v12, 6, v0
	v_bfe_u32 v131, v0, 4, 2
	v_and_b32_e32 v106, 15, v0
	v_lshlrev_b32_e32 v107, 5, v12
	v_or_b32_e32 v73, v107, v106
	v_lshlrev_b32_e32 v60, 5, v131
	v_mov_b32_e32 v61, 0
	v_lshl_add_u64 v[42:43], s[30:31], 0, v[60:61]
	v_lshlrev_b32_e32 v2, 7, v73
	v_mov_b32_e32 v3, v61
	v_lshl_add_u64 v[10:11], v[42:43], 0, v[2:3]
	v_lshl_add_u64 v[50:51], s[18:19], 0, v[60:61]
	global_load_dwordx4 v[2:5], v[10:11], off offset:16
	global_load_dwordx4 v[6:9], v[10:11], off
	v_lshlrev_b32_e32 v10, 9, v73
	v_mov_b32_e32 v11, v61
	v_lshl_add_u64 v[34:35], v[50:51], 0, v[10:11]
	v_lshlrev_b32_e32 v62, 7, v12
	v_mov_b32_e32 v63, v61
	v_lshl_add_u64 v[18:19], v[34:35], 0, v[62:63]
	global_load_dwordx4 v[10:13], v[18:19], off offset:16
	global_load_dwordx4 v[14:17], v[18:19], off
	v_add_u32_e32 v18, 32, v107
	v_and_b32_e32 v108, 0x60, v18
	v_lshlrev_b32_e32 v64, 2, v108
	v_mov_b32_e32 v65, v61
	v_lshl_add_u64 v[26:27], v[34:35], 0, v[64:65]
	v_xor_b32_e32 v109, 64, v107
	global_load_dwordx4 v[18:21], v[26:27], off offset:16
	global_load_dwordx4 v[22:25], v[26:27], off
	v_lshlrev_b32_e32 v66, 2, v109
	v_mov_b32_e32 v67, v61
	v_lshl_add_u64 v[36:37], v[34:35], 0, v[66:67]
	global_load_dwordx4 v[26:29], v[36:37], off
	global_load_dwordx4 v[30:33], v[36:37], off offset:16
	v_add_u32_e32 v36, 0x60, v107
	v_and_b32_e32 v111, 0x60, v36
	v_mov_b32_e32 v69, v61
	v_lshlrev_b32_e32 v68, 2, v111
	v_lshl_add_u64 v[44:45], v[34:35], 0, v[68:69]
	global_load_dwordx4 v[34:37], v[44:45], off
	global_load_dwordx4 v[38:41], v[44:45], off offset:16
	v_or_b32_e32 v54, 16, v73
	v_mov_b32_e32 v45, v61
	v_lshlrev_b32_e32 v44, 7, v54
	v_lshl_add_u64 v[52:53], v[42:43], 0, v[44:45]
	global_load_dwordx4 v[42:45], v[52:53], off
	global_load_dwordx4 v[46:49], v[52:53], off offset:16
	v_mov_b32_e32 v53, v61
	v_lshlrev_b32_e32 v52, 9, v54
	v_lshl_add_u64 v[58:59], v[50:51], 0, v[52:53]
	v_lshl_add_u64 v[70:71], v[58:59], 0, v[62:63]
	global_load_dwordx4 v[50:53], v[70:71], off
	global_load_dwordx4 v[54:57], v[70:71], off offset:16
	v_lshl_add_u64 v[70:71], v[58:59], 0, v[64:65]
	v_lshl_add_u64 v[98:99], v[58:59], 0, v[66:67]
	v_lshl_add_u64 v[58:59], v[58:59], 0, v[68:69]
	global_load_dwordx4 v[74:77], v[70:71], off offset:16
	global_load_dwordx4 v[78:81], v[70:71], off
	global_load_dwordx4 v[82:85], v[98:99], off offset:16
	global_load_dwordx4 v[86:89], v[98:99], off
	global_load_dwordx4 v[90:93], v[58:59], off offset:16
	global_load_dwordx4 v[94:97], v[58:59], off
	s_mov_b32 s0, 0x3fb8aa3b
	v_lshlrev_b32_e32 v72, 9, v0
	v_and_b32_e32 v1, 16, v1
	v_or3_b32 v107, v106, v1, v107
	v_lshlrev_b32_e32 v107, 1, v107
	s_mov_b32 s3, 32
	v_cmp_eq_u32_e64 s[4:5], 3, v131
	s_waitcnt vmcnt(19)
	v_pk_mul_f32 v[58:59], v[2:3], s[0:1] op_sel_hi:[1,0]
	s_waitcnt vmcnt(18)
	v_pk_mul_f32 v[6:7], v[6:7], s[0:1] op_sel_hi:[1,0]
	v_pk_mul_f32 v[8:9], v[8:9], s[0:1] op_sel_hi:[1,0]
	v_cvt_pk_f16_f32 v2, v6, v7
	v_cvt_pk_f16_f32 v3, v8, v9
	v_pk_mul_f32 v[70:71], v[4:5], s[0:1] op_sel_hi:[1,0]
	v_cvt_pk_f16_f32 v4, v58, v59
	s_waitcnt vmcnt(17)
	v_cvt_f16_f32_e32 v13, v13
	s_waitcnt vmcnt(16)
	v_cvt_f16_f32_e32 v6, v14
	v_cvt_pk_f16_f32 v8, v17, v10
	v_cvt_pk_f16_f32 v5, v70, v71
	v_lshl_add_u64 v[70:71], s[22:23], 0, v[60:61]
	v_and_b32_e32 v60, 0x19e00, v72
	v_cvt_pk_f16_f32 v9, v15, v16
	s_waitcnt vmcnt(15)
	v_cvt_f16_f32_e32 v17, v21
	v_cvt_pk_f16_f32 v10, v11, v12
	s_waitcnt vmcnt(14)
	v_cvt_f16_f32_e32 v14, v22
	v_cvt_pk_f16_f32 v15, v23, v24
	v_cvt_pk_f16_f32 v12, v25, v18
	v_cvt_pk_f16_f32 v16, v19, v20
	v_lshl_add_u64 v[58:59], v[70:71], 0, v[60:61]
	s_waitcnt vmcnt(13)
	v_cvt_f16_f32_e32 v18, v26
	v_alignbit_b32 v7, v8, v9, 16
	v_alignbit_b32 v11, v12, v15, 16
	v_alignbit_b32 v12, v16, v12, 16
	v_pack_b32_f16 v6, v6, v9
	v_alignbit_b32 v9, v13, v10, 16
	v_alignbit_b32 v13, v17, v16, 16
	v_lshl_add_u64 v[16:17], v[58:59], 0, v[62:63]
	global_load_dwordx4 v[98:101], v[16:17], off offset:16
	global_load_dwordx4 v[102:105], v[16:17], off
	s_waitcnt vmcnt(14)
	v_cvt_f16_f32_e32 v17, v33
	s_waitcnt vmcnt(13)
	v_cvt_f16_f32_e32 v20, v34
	v_alignbit_b32 v8, v10, v8, 16
	v_pack_b32_f16 v10, v14, v15
	v_cvt_pk_f16_f32 v15, v27, v28
	v_pack_b32_f16 v14, v18, v15
	v_cvt_pk_f16_f32 v18, v29, v30
	v_cvt_pk_f16_f32 v19, v31, v32
	v_alignbit_b32 v16, v19, v18, 16
	v_alignbit_b32 v17, v17, v19, 16
	v_cvt_pk_f16_f32 v19, v35, v36
	v_alignbit_b32 v15, v18, v15, 16
	v_pack_b32_f16 v18, v20, v19
	v_lshl_add_u64 v[20:21], v[58:59], 0, v[64:65]
	global_load_dwordx4 v[112:115], v[20:21], off offset:16
	global_load_dwordx4 v[116:119], v[20:21], off
	s_waitcnt vmcnt(14)
	v_cvt_f16_f32_e32 v21, v41
	v_lshl_add_u64 v[26:27], v[58:59], 0, v[66:67]
	global_load_dwordx4 v[124:127], v[26:27], off offset:16
	global_load_dwordx4 v[132:135], v[26:27], off
	v_cvt_pk_f16_f32 v20, v37, v38
	v_cvt_pk_f16_f32 v22, v39, v40
	s_waitcnt vmcnt(13)
	v_cvt_f16_f32_e32 v28, v50
	v_alignbit_b32 v19, v20, v19, 16
	v_alignbit_b32 v20, v22, v20, 16
	v_alignbit_b32 v21, v21, v22, 16
	v_pk_mul_f32 v[22:23], v[42:43], s[0:1] op_sel_hi:[1,0]
	v_pk_mul_f32 v[24:25], v[44:45], s[0:1] op_sel_hi:[1,0]
	v_cvt_pk_f16_f32 v22, v22, v23
	v_cvt_pk_f16_f32 v23, v24, v25
	v_pk_mul_f32 v[24:25], v[46:47], s[0:1] op_sel_hi:[1,0]
	v_pk_mul_f32 v[26:27], v[48:49], s[0:1] op_sel_hi:[1,0]
	v_cvt_pk_f16_f32 v24, v24, v25
	v_cvt_pk_f16_f32 v25, v26, v27
	v_cvt_pk_f16_f32 v27, v51, v52
	s_waitcnt vmcnt(12)
	v_cvt_f16_f32_e32 v31, v57
	v_pack_b32_f16 v26, v28, v27
	v_lshl_add_u64 v[28:29], v[58:59], 0, v[68:69]
	global_load_dwordx4 v[140:143], v[28:29], off offset:16
	global_load_dwordx4 v[144:147], v[28:29], off
	s_mov_b64 s[0:1], 0x2000
	v_cvt_pk_f16_f32 v30, v53, v54
	v_cvt_pk_f16_f32 v29, v55, v56
	v_lshl_add_u64 v[46:47], v[58:59], 0, s[0:1]
	v_alignbit_b32 v27, v30, v27, 16
	v_alignbit_b32 v28, v29, v30, 16
	v_alignbit_b32 v29, v31, v29, 16
	v_lshl_add_u64 v[30:31], v[46:47], 0, v[62:63]
	global_load_dwordx4 v[148:151], v[30:31], off offset:16
	global_load_dwordx4 v[152:155], v[30:31], off
	s_waitcnt vmcnt(14)
	v_cvt_f16_f32_e32 v32, v78
	v_cvt_f16_f32_e32 v33, v77
	s_waitcnt vmcnt(12)
	v_cvt_f16_f32_e32 v35, v86
	v_cvt_pk_f16_f32 v31, v79, v80
	v_pack_b32_f16 v30, v32, v31
	v_cvt_pk_f16_f32 v32, v81, v74
	v_cvt_pk_f16_f32 v34, v75, v76
	v_cvt_pk_f16_f32 v36, v87, v88
	v_cvt_pk_f16_f32 v38, v89, v82
	v_alignbit_b32 v31, v32, v31, 16
	v_alignbit_b32 v32, v34, v32, 16
	v_alignbit_b32 v33, v33, v34, 16
	v_pack_b32_f16 v34, v35, v36
	v_alignbit_b32 v35, v38, v36, 16
	v_lshl_add_u64 v[36:37], v[46:47], 0, v[64:65]
	global_load_dwordx4 v[74:77], v[36:37], off offset:16
	global_load_dwordx4 v[78:81], v[36:37], off
	v_cvt_f16_f32_e32 v37, v85
	s_waitcnt vmcnt(12)
	v_cvt_f16_f32_e32 v40, v94
	v_cvt_f16_f32_e32 v44, v93
	v_cvt_pk_f16_f32 v39, v83, v84
	v_alignbit_b32 v36, v39, v38, 16
	v_alignbit_b32 v37, v37, v39, 16
	v_cvt_pk_f16_f32 v39, v95, v96
	v_pack_b32_f16 v38, v40, v39
	v_cvt_pk_f16_f32 v42, v97, v90
	v_cvt_pk_f16_f32 v43, v91, v92
	v_lshl_add_u64 v[40:41], v[46:47], 0, v[66:67]
	v_alignbit_b32 v39, v42, v39, 16
	global_load_dwordx4 v[82:85], v[40:41], off offset:16
	global_load_dwordx4 v[86:89], v[40:41], off
	v_alignbit_b32 v40, v43, v42, 16
	v_alignbit_b32 v41, v44, v43, 16
	v_lshl_add_u64 v[46:47], v[46:47], 0, v[68:69]
	s_mov_b64 s[0:1], 0x4000
	s_waitcnt vmcnt(12)
	v_pk_add_f32 v[42:43], v[102:103], v[102:103]
	v_pk_add_f32 v[44:45], v[104:105], v[104:105]
	v_cvt_pk_f16_f32 v42, v42, v43
	v_cvt_pk_f16_f32 v43, v44, v45
	v_pk_add_f32 v[44:45], v[98:99], v[98:99]
	global_load_dwordx4 v[90:93], v[46:47], off offset:16
	global_load_dwordx4 v[94:97], v[46:47], off
	v_pk_add_f32 v[46:47], v[100:101], v[100:101]
	v_lshl_add_u64 v[120:121], v[58:59], 0, s[0:1]
	v_cvt_pk_f16_f32 v44, v44, v45
	v_cvt_pk_f16_f32 v45, v46, v47
	v_lshl_add_u64 v[50:51], v[120:121], 0, v[62:63]
	global_load_dwordx4 v[98:101], v[50:51], off offset:16
	global_load_dwordx4 v[102:105], v[50:51], off
	v_lshl_add_u64 v[58:59], v[120:121], 0, v[66:67]
	v_or_b32_e32 v60, 0x6000, v72
	s_waitcnt vmcnt(15)
	v_pk_add_f32 v[50:51], v[114:115], v[114:115]
	s_waitcnt vmcnt(14)
	v_pk_add_f32 v[46:47], v[116:117], v[116:117]
	v_pk_add_f32 v[48:49], v[118:119], v[118:119]
	v_cvt_pk_f16_f32 v46, v46, v47
	v_cvt_pk_f16_f32 v47, v48, v49
	v_pk_add_f32 v[48:49], v[112:113], v[112:113]
	s_waitcnt vmcnt(12)
	v_pk_add_f32 v[52:53], v[134:135], v[134:135]
	v_cvt_pk_f16_f32 v48, v48, v49
	v_cvt_pk_f16_f32 v49, v50, v51
	v_pk_add_f32 v[50:51], v[132:133], v[132:133]
	v_pk_add_f32 v[54:55], v[126:127], v[126:127]
	v_cvt_pk_f16_f32 v50, v50, v51
	v_cvt_pk_f16_f32 v51, v52, v53
	v_pk_add_f32 v[52:53], v[124:125], v[124:125]
	v_lshl_add_u64 v[70:71], v[70:71], 0, v[60:61]
	v_cvt_pk_f16_f32 v52, v52, v53
	v_cvt_pk_f16_f32 v53, v54, v55
	v_lshl_add_u64 v[54:55], v[120:121], 0, v[64:65]
	global_load_dwordx4 v[112:115], v[54:55], off offset:16
	global_load_dwordx4 v[116:119], v[54:55], off
	global_load_dwordx4 v[124:127], v[58:59], off offset:16
	global_load_dwordx4 v[132:135], v[58:59], off
	v_lshl_add_u64 v[120:121], v[120:121], 0, v[68:69]
	v_lshl_add_u64 v[60:61], v[70:71], 0, v[62:63]
	s_waitcnt vmcnt(15)
	v_pk_add_f32 v[58:59], v[142:143], v[142:143]
	s_waitcnt vmcnt(14)
	v_pk_add_f32 v[54:55], v[144:145], v[144:145]
	v_pk_add_f32 v[56:57], v[146:147], v[146:147]
	v_cvt_pk_f16_f32 v54, v54, v55
	v_cvt_pk_f16_f32 v55, v56, v57
	v_pk_add_f32 v[56:57], v[140:141], v[140:141]
	global_load_dwordx4 v[140:143], v[120:121], off offset:16
	global_load_dwordx4 v[144:147], v[120:121], off
	v_cvt_pk_f16_f32 v56, v56, v57
	v_cvt_pk_f16_f32 v57, v58, v59
	v_lshl_add_u64 v[64:65], v[70:71], 0, v[64:65]
	s_waitcnt vmcnt(14)
	v_pk_add_f32 v[58:59], v[152:153], v[152:153]
	v_pk_add_f32 v[120:121], v[154:155], v[154:155]
	global_load_dwordx4 v[152:155], v[60:61], off offset:16
	global_load_dwordx4 v[156:159], v[60:61], off
	v_cvt_pk_f16_f32 v58, v58, v59
	v_cvt_pk_f16_f32 v59, v120, v121
	v_pk_add_f32 v[120:121], v[148:149], v[148:149]
	v_pk_add_f32 v[62:63], v[150:151], v[150:151]
	global_load_dwordx4 v[148:151], v[64:65], off offset:16
	global_load_dwordx4 v[160:163], v[64:65], off
	v_lshl_add_u64 v[66:67], v[70:71], 0, v[66:67]
	global_load_dwordx4 v[164:167], v[66:67], off offset:16
	global_load_dwordx4 v[168:171], v[66:67], off
	v_lshl_add_u64 v[68:69], v[70:71], 0, v[68:69]
	global_load_dwordx4 v[172:175], v[68:69], off offset:16
	global_load_dwordx4 v[176:179], v[68:69], off
	v_cvt_pk_f16_f32 v60, v120, v121
	v_cvt_pk_f16_f32 v61, v62, v63
	v_lshlrev_b32_e32 v120, 2, v73
	v_and_b32_e32 v73, 0xcf, v0
	s_waitcnt vmcnt(20)
	v_pk_add_f32 v[62:63], v[78:79], v[78:79]
	v_pk_add_f32 v[64:65], v[80:81], v[80:81]
	v_cvt_pk_f16_f32 v62, v62, v63
	v_cvt_pk_f16_f32 v63, v64, v65
	v_pk_add_f32 v[64:65], v[74:75], v[74:75]
	v_pk_add_f32 v[74:75], v[76:77], v[76:77]
	v_lshlrev_b32_e32 v76, 2, v73
	v_mov_b32_e32 v77, 0xc0
	global_load_dword v110, v120, s[20:21]
	global_load_dword v121, v120, s[20:21] offset:64
	global_load_dword v122, v76, s[8:9]
	v_lshl_or_b32 v77, v0, 2, v77
	global_load_dword v128, v76, s[8:9] offset:64
	global_load_dword v129, v76, s[8:9] offset:128
	global_load_dword v130, v77, s[8:9]
	v_cvt_pk_f16_f32 v64, v64, v65
	v_cvt_pk_f16_f32 v65, v74, v75
	s_waitcnt vmcnt(24)
	v_pk_add_f32 v[66:67], v[86:87], v[86:87]
	v_pk_add_f32 v[74:75], v[88:89], v[88:89]
	v_pk_add_f32 v[68:69], v[82:83], v[82:83]
	v_pk_add_f32 v[70:71], v[84:85], v[84:85]
	v_cvt_pk_f16_f32 v66, v66, v67
	v_cvt_pk_f16_f32 v67, v74, v75
	v_cvt_pk_f16_f32 v68, v68, v69
	v_cvt_pk_f16_f32 v69, v70, v71
	s_movk_i32 s0, 0xc0
	s_waitcnt vmcnt(22)
	v_pk_add_f32 v[70:71], v[94:95], v[94:95]
	v_pk_add_f32 v[74:75], v[96:97], v[96:97]
	v_cvt_pk_f16_f32 v70, v70, v71
	v_cvt_pk_f16_f32 v71, v74, v75
	v_pk_add_f32 v[74:75], v[90:91], v[90:91]
	s_waitcnt vmcnt(21)
	v_pk_add_f32 v[78:79], v[100:101], v[100:101]
	v_cvt_pk_f16_f32 v72, v74, v75
	v_pk_add_f32 v[74:75], v[92:93], v[92:93]
	s_waitcnt vmcnt(20)
	v_pk_add_f32 v[76:77], v[104:105], v[104:105]
	v_cvt_pk_f16_f32 v73, v74, v75
	v_pk_add_f32 v[74:75], v[102:103], v[102:103]
	v_mov_b32_e32 v186, 0
	v_mov_b32_e32 v187, 0
	v_mov_b32_e32 v188, 0
	v_mov_b32_e32 v189, 0
	v_mov_b32_e32 v190, 0x13480
	ds_write_b128 v190, v[186:189]
	s_waitcnt lgkmcnt(0)
	v_cvt_pk_f16_f32 v74, v74, v75
	v_cvt_pk_f16_f32 v75, v76, v77
	v_pk_add_f32 v[76:77], v[98:99], v[98:99]
	s_barrier
	v_cvt_pk_f16_f32 v76, v76, v77
	v_cvt_pk_f16_f32 v77, v78, v79
	s_waitcnt vmcnt(19)
	v_pk_add_f32 v[82:83], v[114:115], v[114:115]
	s_waitcnt vmcnt(18)
	v_pk_add_f32 v[78:79], v[116:117], v[116:117]
	v_pk_add_f32 v[80:81], v[118:119], v[118:119]
	v_cvt_pk_f16_f32 v78, v78, v79
	v_cvt_pk_f16_f32 v79, v80, v81
	v_pk_add_f32 v[80:81], v[112:113], v[112:113]
	s_waitcnt vmcnt(16)
	v_pk_add_f32 v[84:85], v[134:135], v[134:135]
	v_cvt_pk_f16_f32 v80, v80, v81
	v_cvt_pk_f16_f32 v81, v82, v83
	v_pk_add_f32 v[82:83], v[132:133], v[132:133]
	v_pk_add_f32 v[86:87], v[126:127], v[126:127]
	v_cvt_pk_f16_f32 v82, v82, v83
	v_cvt_pk_f16_f32 v83, v84, v85
	v_pk_add_f32 v[84:85], v[124:125], v[124:125]
	s_waitcnt vmcnt(14)
	v_pk_add_f32 v[88:89], v[146:147], v[146:147]
	v_cvt_pk_f16_f32 v84, v84, v85
	v_cvt_pk_f16_f32 v85, v86, v87
	v_pk_add_f32 v[86:87], v[144:145], v[144:145]
	v_pk_add_f32 v[90:91], v[142:143], v[142:143]
	v_cvt_pk_f16_f32 v86, v86, v87
	v_cvt_pk_f16_f32 v87, v88, v89
	v_pk_add_f32 v[88:89], v[140:141], v[140:141]
	s_waitcnt vmcnt(12)
	v_pk_add_f32 v[92:93], v[158:159], v[158:159]
	v_cvt_pk_f16_f32 v88, v88, v89
	v_cvt_pk_f16_f32 v89, v90, v91
	v_pk_add_f32 v[90:91], v[156:157], v[156:157]
	v_pk_add_f32 v[94:95], v[154:155], v[154:155]
	v_cvt_pk_f16_f32 v90, v90, v91
	v_cvt_pk_f16_f32 v91, v92, v93
	v_pk_add_f32 v[92:93], v[152:153], v[152:153]
	s_waitcnt vmcnt(10)
	v_pk_add_f32 v[96:97], v[162:163], v[162:163]
	v_cvt_pk_f16_f32 v92, v92, v93
	v_cvt_pk_f16_f32 v93, v94, v95
	v_pk_add_f32 v[94:95], v[160:161], v[160:161]
	v_pk_add_f32 v[98:99], v[150:151], v[150:151]
	v_cvt_pk_f16_f32 v94, v94, v95
	v_cvt_pk_f16_f32 v95, v96, v97
	v_pk_add_f32 v[96:97], v[148:149], v[148:149]
	s_waitcnt vmcnt(8)
	v_pk_add_f32 v[100:101], v[170:171], v[170:171]
	v_cvt_pk_f16_f32 v96, v96, v97
	v_cvt_pk_f16_f32 v97, v98, v99
	v_pk_add_f32 v[98:99], v[168:169], v[168:169]
	v_pk_add_f32 v[102:103], v[166:167], v[166:167]
	v_cvt_pk_f16_f32 v98, v98, v99
	v_cvt_pk_f16_f32 v99, v100, v101
	v_pk_add_f32 v[100:101], v[164:165], v[164:165]
	s_waitcnt vmcnt(6)
	v_pk_add_f32 v[104:105], v[178:179], v[178:179]
	v_cvt_pk_f16_f32 v100, v100, v101
	v_cvt_pk_f16_f32 v101, v102, v103
	v_pk_add_f32 v[102:103], v[176:177], v[176:177]
	v_lshlrev_b32_e32 v115, 4, v131
	v_cvt_pk_f16_f32 v102, v102, v103
	v_cvt_pk_f16_f32 v103, v104, v105
	v_pk_add_f32 v[104:105], v[172:173], v[172:173]
	v_pk_add_f32 v[112:113], v[174:175], v[174:175]
	v_and_or_b32 v116, v0, s0, v115
	v_cvt_pk_f16_f32 v104, v104, v105
	v_cvt_pk_f16_f32 v105, v112, v113
	v_or_b32_e32 v1, v116, v106
	v_add_u32_e32 v112, 0x129c0, v120
	ds_read2_b32 v[112:113], v112 offset1:16
	v_lshrrev_b32_e32 v117, 3, v1
	v_mov_b32_e32 v1, 0x133c0
	v_lshl_or_b32 v108, v108, 1, v115
	v_lshl_or_b32 v109, v109, 1, v115
	v_lshl_or_b32 v111, v111, 1, v115
	v_add_u32_e32 v148, 0x131c0, v107
	v_add_u32_e32 v149, 0x132c0, v107
	v_mov_b32_e32 v107, 0x13440
	v_lshl_add_u32 v1, v117, 2, v1
	v_add_u32_e32 v139, 0x131c0, v116
	v_add_u32_e32 v140, 0x131c0, v108
	v_add_u32_e32 v141, 0x131c0, v109
	v_add_u32_e32 v142, 0x131c0, v111
	v_add_u32_e32 v143, 0x132c0, v116
	v_add_u32_e32 v144, 0x132c0, v108
	v_add_u32_e32 v145, 0x132c0, v109
	v_add_u32_e32 v146, 0x132c0, v111
	v_or_b32_e32 v147, 0x13440, v115
	v_lshl_or_b32 v150, v117, 1, v107
	v_lshlrev_b32_e32 v151, 2, v123
	ds_read_b32 v152, v1
	ds_read_b32 v153, v151
	s_waitcnt vmcnt(5)
	v_mul_f32_e32 v106, 0x3fb8aa3b, v110
	s_waitcnt vmcnt(4)
	v_mul_f32_e32 v110, 0x3fb8aa3b, v121
	s_waitcnt vmcnt(3)
	v_mul_f32_e32 v114, 0x4038aa3b, v122
	s_waitcnt vmcnt(2)
	v_mul_f32_e32 v118, 0x4038aa3b, v128
	s_waitcnt vmcnt(1)
	v_mul_f32_e32 v122, 0x4038aa3b, v129
	s_waitcnt vmcnt(0)
	v_mul_f32_e32 v126, 0x4038aa3b, v130
	s_waitcnt lgkmcnt(2)
	v_mul_f32_e32 v130, 0x3fb8aa3b, v112
	v_mul_f32_e32 v134, 0x3fb8aa3b, v113
	v_cmp_lt_u32_e64 s[0:1], 1, v131
	v_and_b32_e32 v132, 16, v0
	v_mov_b32_e32 v107, 0
	v_cndmask_b32_e64 v154, v130, v134, s[0:1]
	v_mov_b32_e32 v108, 0
	v_mov_b32_e32 v109, 0
	v_mov_b32_e32 v111, 0
	v_mov_b32_e32 v112, 0
	v_mov_b32_e32 v113, 0
	v_mov_b32_e32 v115, 0
	v_mov_b32_e32 v116, 0
	v_mov_b32_e32 v117, 0
	v_mov_b32_e32 v119, 0
	v_mov_b32_e32 v120, 0
	v_mov_b32_e32 v121, 0
	v_mov_b32_e32 v123, 0
	v_mov_b32_e32 v124, 0
	v_mov_b32_e32 v125, 0
	v_mov_b32_e32 v127, 0
	v_mov_b32_e32 v128, 0
	v_mov_b32_e32 v129, 0
	v_cmp_eq_u32_e64 s[6:7], 0, v132
	v_mov_b32_e32 v135, 0
	v_mov_b32_e32 v136, 0
	v_mov_b32_e32 v137, 0
	v_mov_b32_e32 v131, 0
	v_mov_b32_e32 v132, 0
	v_mov_b32_e32 v133, 0
	v_and_b32_e32 v187, 2, v0
	v_and_b32_e32 v188, 1, v0
	v_cmp_ne_u32_e64 s[46:47], 0, v187
	v_cmp_ne_u32_e64 s[48:49], 0, v188
	v_mov_b32_e32 v189, 0x44444444
	v_mov_b32_e32 v191, 0xeeeeeeee
	v_cndmask_b32_e64 v191, v189, v191, s[48:49]
	v_cndmask_b32_e64 v139, v139, v190, s[46:47]
	v_cndmask_b32_e64 v140, v140, v190, s[46:47]
	v_cndmask_b32_e64 v141, v141, v190, s[46:47]
	v_cndmask_b32_e64 v142, v142, v190, s[46:47]
	v_cndmask_b32_e64 v143, v143, v190, s[46:47]
	v_cndmask_b32_e64 v144, v144, v190, s[46:47]
	v_cndmask_b32_e64 v145, v145, v190, s[46:47]
	v_cndmask_b32_e64 v146, v146, v190, s[46:47]
	v_cndmask_b32_e64 v147, v147, v190, s[46:47]
	v_mov_b32_e32 v192, 0
	v_mov_b32_e32 v193, 0
	v_mov_b32_e32 v194, 0
	v_mov_b32_e32 v195, 0
	v_mov_b32_e32 v196, 0
	v_mov_b32_e32 v197, 0
	v_mov_b32_e32 v198, 0
	v_mov_b32_e32 v199, 0
	v_mov_b32_e32 v200, 0
	v_mov_b32_e32 v201, 0
	v_mov_b32_e32 v202, 0
	v_mov_b32_e32 v203, 0
	v_mov_b32_e32 v204, 0
	v_mov_b32_e32 v205, 0
	v_mov_b32_e32 v206, 0
	v_mov_b32_e32 v207, 0
	v_and_b32_e32 v240, 15, v0
	v_bfe_u32 v241, v0, 5, 1
	v_lshl_add_u32 v242, v241, 4, v240
	v_lshlrev_b32_e32 v242, 2, v242
	v_add_u32_e32 v243, 128, v242
	v_and_b32_e32 v241, 16, v0
	v_cmp_ne_u32_e64 s[50:51], 0, v241
	ds_bpermute_b32 v244, v242, v6
	ds_bpermute_b32 v245, v242, v8
	s_waitcnt lgkmcnt(0)
	v_cndmask_b32_e64 v208, v244, v245, s[50:51]
	ds_bpermute_b32 v244, v242, v26
	ds_bpermute_b32 v245, v242, v28
	s_waitcnt lgkmcnt(0)
	v_cndmask_b32_e64 v209, v244, v245, s[50:51]
	ds_bpermute_b32 v244, v242, v7
	ds_bpermute_b32 v245, v242, v9
	s_waitcnt lgkmcnt(0)
	v_cndmask_b32_e64 v210, v244, v245, s[50:51]
	ds_bpermute_b32 v244, v242, v27
	ds_bpermute_b32 v245, v242, v29
	s_waitcnt lgkmcnt(0)
	v_cndmask_b32_e64 v211, v244, v245, s[50:51]
	ds_bpermute_b32 v244, v243, v6
	ds_bpermute_b32 v245, v243, v8
	s_waitcnt lgkmcnt(0)
	v_cndmask_b32_e64 v212, v244, v245, s[50:51]
	ds_bpermute_b32 v244, v243, v26
	ds_bpermute_b32 v245, v243, v28
	s_waitcnt lgkmcnt(0)
	v_cndmask_b32_e64 v213, v244, v245, s[50:51]
	ds_bpermute_b32 v244, v243, v7
	ds_bpermute_b32 v245, v243, v9
	s_waitcnt lgkmcnt(0)
	v_cndmask_b32_e64 v214, v244, v245, s[50:51]
	ds_bpermute_b32 v244, v243, v27
	ds_bpermute_b32 v245, v243, v29
	s_waitcnt lgkmcnt(0)
	v_cndmask_b32_e64 v215, v244, v245, s[50:51]
	ds_bpermute_b32 v244, v242, v10
	ds_bpermute_b32 v245, v242, v12
	s_waitcnt lgkmcnt(0)
	v_cndmask_b32_e64 v216, v244, v245, s[50:51]
	ds_bpermute_b32 v244, v242, v30
	ds_bpermute_b32 v245, v242, v32
	s_waitcnt lgkmcnt(0)
	v_cndmask_b32_e64 v217, v244, v245, s[50:51]
	ds_bpermute_b32 v244, v242, v11
	ds_bpermute_b32 v245, v242, v13
	s_waitcnt lgkmcnt(0)
	v_cndmask_b32_e64 v218, v244, v245, s[50:51]
	ds_bpermute_b32 v244, v242, v31
	ds_bpermute_b32 v245, v242, v33
	s_waitcnt lgkmcnt(0)
	v_cndmask_b32_e64 v219, v244, v245, s[50:51]
	ds_bpermute_b32 v244, v243, v10
	ds_bpermute_b32 v245, v243, v12
	s_waitcnt lgkmcnt(0)
	v_cndmask_b32_e64 v220, v244, v245, s[50:51]
	ds_bpermute_b32 v244, v243, v30
	ds_bpermute_b32 v245, v243, v32
	s_waitcnt lgkmcnt(0)
	v_cndmask_b32_e64 v221, v244, v245, s[50:51]
	ds_bpermute_b32 v244, v243, v11
	ds_bpermute_b32 v245, v243, v13
	s_waitcnt lgkmcnt(0)
	v_cndmask_b32_e64 v222, v244, v245, s[50:51]
	ds_bpermute_b32 v244, v243, v31
	ds_bpermute_b32 v245, v243, v33
	s_waitcnt lgkmcnt(0)
	v_cndmask_b32_e64 v223, v244, v245, s[50:51]
	ds_bpermute_b32 v244, v242, v14
	ds_bpermute_b32 v245, v242, v16
	s_waitcnt lgkmcnt(0)
	v_cndmask_b32_e64 v224, v244, v245, s[50:51]
	ds_bpermute_b32 v244, v242, v34
	ds_bpermute_b32 v245, v242, v36
	s_waitcnt lgkmcnt(0)
	v_cndmask_b32_e64 v225, v244, v245, s[50:51]
	ds_bpermute_b32 v244, v242, v15
	ds_bpermute_b32 v245, v242, v17
	s_waitcnt lgkmcnt(0)
	v_cndmask_b32_e64 v226, v244, v245, s[50:51]
	ds_bpermute_b32 v244, v242, v35
	ds_bpermute_b32 v245, v242, v37
	s_waitcnt lgkmcnt(0)
	v_cndmask_b32_e64 v227, v244, v245, s[50:51]
	ds_bpermute_b32 v244, v243, v14
	ds_bpermute_b32 v245, v243, v16
	s_waitcnt lgkmcnt(0)
	v_cndmask_b32_e64 v228, v244, v245, s[50:51]
	ds_bpermute_b32 v244, v243, v34
	ds_bpermute_b32 v245, v243, v36
	s_waitcnt lgkmcnt(0)
	v_cndmask_b32_e64 v229, v244, v245, s[50:51]
	ds_bpermute_b32 v244, v243, v15
	ds_bpermute_b32 v245, v243, v17
	s_waitcnt lgkmcnt(0)
	v_cndmask_b32_e64 v230, v244, v245, s[50:51]
	ds_bpermute_b32 v244, v243, v35
	ds_bpermute_b32 v245, v243, v37
	s_waitcnt lgkmcnt(0)
	v_cndmask_b32_e64 v231, v244, v245, s[50:51]
	ds_bpermute_b32 v244, v242, v18
	ds_bpermute_b32 v245, v242, v20
	s_waitcnt lgkmcnt(0)
	v_cndmask_b32_e64 v232, v244, v245, s[50:51]
	ds_bpermute_b32 v244, v242, v38
	ds_bpermute_b32 v245, v242, v40
	s_waitcnt lgkmcnt(0)
	v_cndmask_b32_e64 v233, v244, v245, s[50:51]
	ds_bpermute_b32 v244, v242, v19
	ds_bpermute_b32 v245, v242, v21
	s_waitcnt lgkmcnt(0)
	v_cndmask_b32_e64 v234, v244, v245, s[50:51]
	ds_bpermute_b32 v244, v242, v39
	ds_bpermute_b32 v245, v242, v41
	s_waitcnt lgkmcnt(0)
	v_cndmask_b32_e64 v235, v244, v245, s[50:51]
	ds_bpermute_b32 v244, v243, v18
	ds_bpermute_b32 v245, v243, v20
	s_waitcnt lgkmcnt(0)
	v_cndmask_b32_e64 v236, v244, v245, s[50:51]
	ds_bpermute_b32 v244, v243, v38
	ds_bpermute_b32 v245, v243, v40
	s_waitcnt lgkmcnt(0)
	v_cndmask_b32_e64 v237, v244, v245, s[50:51]
	ds_bpermute_b32 v244, v243, v19
	ds_bpermute_b32 v245, v243, v21
	s_waitcnt lgkmcnt(0)
	v_cndmask_b32_e64 v238, v244, v245, s[50:51]
	ds_bpermute_b32 v244, v243, v39
	ds_bpermute_b32 v245, v243, v41
	s_waitcnt lgkmcnt(0)
	v_cndmask_b32_e64 v239, v244, v245, s[50:51]
	v_mov_b32_e32 v6, v208
	v_mov_b32_e32 v7, v209
	v_mov_b32_e32 v8, v210
	v_mov_b32_e32 v9, v211
	v_mov_b32_e32 v10, v212
	v_mov_b32_e32 v11, v213
	v_mov_b32_e32 v12, v214
	v_mov_b32_e32 v13, v215
	v_mov_b32_e32 v14, v216
	v_mov_b32_e32 v15, v217
	v_mov_b32_e32 v16, v218
	v_mov_b32_e32 v17, v219
	v_mov_b32_e32 v18, v220
	v_mov_b32_e32 v19, v221
	v_mov_b32_e32 v20, v222
	v_mov_b32_e32 v21, v223
	v_mov_b32_e32 v26, v224
	v_mov_b32_e32 v27, v225
	v_mov_b32_e32 v28, v226
	v_mov_b32_e32 v29, v227
	v_mov_b32_e32 v30, v228
	v_mov_b32_e32 v31, v229
	v_mov_b32_e32 v32, v230
	v_mov_b32_e32 v33, v231
	v_mov_b32_e32 v34, v232
	v_mov_b32_e32 v35, v233
	v_mov_b32_e32 v36, v234
	v_mov_b32_e32 v37, v235
	v_mov_b32_e32 v38, v236
	v_mov_b32_e32 v39, v237
	v_mov_b32_e32 v40, v238
	v_mov_b32_e32 v41, v239
	ds_bpermute_b32 v244, v242, v42
	ds_bpermute_b32 v245, v242, v44
	s_waitcnt lgkmcnt(0)
	v_cndmask_b32_e64 v208, v244, v245, s[50:51]
	ds_bpermute_b32 v244, v242, v58
	ds_bpermute_b32 v245, v242, v60
	s_waitcnt lgkmcnt(0)
	v_cndmask_b32_e64 v209, v244, v245, s[50:51]
	ds_bpermute_b32 v244, v242, v43
	ds_bpermute_b32 v245, v242, v45
	s_waitcnt lgkmcnt(0)
	v_cndmask_b32_e64 v210, v244, v245, s[50:51]
	ds_bpermute_b32 v244, v242, v59
	ds_bpermute_b32 v245, v242, v61
	s_waitcnt lgkmcnt(0)
	v_cndmask_b32_e64 v211, v244, v245, s[50:51]
	ds_bpermute_b32 v244, v243, v42
	ds_bpermute_b32 v245, v243, v44
	s_waitcnt lgkmcnt(0)
	v_cndmask_b32_e64 v212, v244, v245, s[50:51]
	ds_bpermute_b32 v244, v243, v58
	ds_bpermute_b32 v245, v243, v60
	s_waitcnt lgkmcnt(0)
	v_cndmask_b32_e64 v213, v244, v245, s[50:51]
	ds_bpermute_b32 v244, v243, v43
	ds_bpermute_b32 v245, v243, v45
	s_waitcnt lgkmcnt(0)
	v_cndmask_b32_e64 v214, v244, v245, s[50:51]
	ds_bpermute_b32 v244, v243, v59
	ds_bpermute_b32 v245, v243, v61
	s_waitcnt lgkmcnt(0)
	v_cndmask_b32_e64 v215, v244, v245, s[50:51]
	ds_bpermute_b32 v244, v242, v46
	ds_bpermute_b32 v245, v242, v48
	s_waitcnt lgkmcnt(0)
	v_cndmask_b32_e64 v216, v244, v245, s[50:51]
	ds_bpermute_b32 v244, v242, v62
	ds_bpermute_b32 v245, v242, v64
	s_waitcnt lgkmcnt(0)
	v_cndmask_b32_e64 v217, v244, v245, s[50:51]
	ds_bpermute_b32 v244, v242, v47
	ds_bpermute_b32 v245, v242, v49
	s_waitcnt lgkmcnt(0)
	v_cndmask_b32_e64 v218, v244, v245, s[50:51]
	ds_bpermute_b32 v244, v242, v63
	ds_bpermute_b32 v245, v242, v65
	s_waitcnt lgkmcnt(0)
	v_cndmask_b32_e64 v219, v244, v245, s[50:51]
	ds_bpermute_b32 v244, v243, v46
	ds_bpermute_b32 v245, v243, v48
	s_waitcnt lgkmcnt(0)
	v_cndmask_b32_e64 v220, v244, v245, s[50:51]
	ds_bpermute_b32 v244, v243, v62
	ds_bpermute_b32 v245, v243, v64
	s_waitcnt lgkmcnt(0)
	v_cndmask_b32_e64 v221, v244, v245, s[50:51]
	ds_bpermute_b32 v244, v243, v47
	ds_bpermute_b32 v245, v243, v49
	s_waitcnt lgkmcnt(0)
	v_cndmask_b32_e64 v222, v244, v245, s[50:51]
	ds_bpermute_b32 v244, v243, v63
	ds_bpermute_b32 v245, v243, v65
	s_waitcnt lgkmcnt(0)
	v_cndmask_b32_e64 v223, v244, v245, s[50:51]
	ds_bpermute_b32 v244, v242, v50
	ds_bpermute_b32 v245, v242, v52
	s_waitcnt lgkmcnt(0)
	v_cndmask_b32_e64 v224, v244, v245, s[50:51]
	ds_bpermute_b32 v244, v242, v66
	ds_bpermute_b32 v245, v242, v68
	s_waitcnt lgkmcnt(0)
	v_cndmask_b32_e64 v225, v244, v245, s[50:51]
	ds_bpermute_b32 v244, v242, v51
	ds_bpermute_b32 v245, v242, v53
	s_waitcnt lgkmcnt(0)
	v_cndmask_b32_e64 v226, v244, v245, s[50:51]
	ds_bpermute_b32 v244, v242, v67
	ds_bpermute_b32 v245, v242, v69
	s_waitcnt lgkmcnt(0)
	v_cndmask_b32_e64 v227, v244, v245, s[50:51]
	ds_bpermute_b32 v244, v243, v50
	ds_bpermute_b32 v245, v243, v52
	s_waitcnt lgkmcnt(0)
	v_cndmask_b32_e64 v228, v244, v245, s[50:51]
	ds_bpermute_b32 v244, v243, v66
	ds_bpermute_b32 v245, v243, v68
	s_waitcnt lgkmcnt(0)
	v_cndmask_b32_e64 v229, v244, v245, s[50:51]
	ds_bpermute_b32 v244, v243, v51
	ds_bpermute_b32 v245, v243, v53
	s_waitcnt lgkmcnt(0)
	v_cndmask_b32_e64 v230, v244, v245, s[50:51]
	ds_bpermute_b32 v244, v243, v67
	ds_bpermute_b32 v245, v243, v69
	s_waitcnt lgkmcnt(0)
	v_cndmask_b32_e64 v231, v244, v245, s[50:51]
	ds_bpermute_b32 v244, v242, v54
	ds_bpermute_b32 v245, v242, v56
	s_waitcnt lgkmcnt(0)
	v_cndmask_b32_e64 v232, v244, v245, s[50:51]
	ds_bpermute_b32 v244, v242, v70
	ds_bpermute_b32 v245, v242, v72
	s_waitcnt lgkmcnt(0)
	v_cndmask_b32_e64 v233, v244, v245, s[50:51]
	ds_bpermute_b32 v244, v242, v55
	ds_bpermute_b32 v245, v242, v57
	s_waitcnt lgkmcnt(0)
	v_cndmask_b32_e64 v234, v244, v245, s[50:51]
	ds_bpermute_b32 v244, v242, v71
	ds_bpermute_b32 v245, v242, v73
	s_waitcnt lgkmcnt(0)
	v_cndmask_b32_e64 v235, v244, v245, s[50:51]
	ds_bpermute_b32 v244, v243, v54
	ds_bpermute_b32 v245, v243, v56
	s_waitcnt lgkmcnt(0)
	v_cndmask_b32_e64 v236, v244, v245, s[50:51]
	ds_bpermute_b32 v244, v243, v70
	ds_bpermute_b32 v245, v243, v72
	s_waitcnt lgkmcnt(0)
	v_cndmask_b32_e64 v237, v244, v245, s[50:51]
	ds_bpermute_b32 v244, v243, v55
	ds_bpermute_b32 v245, v243, v57
	s_waitcnt lgkmcnt(0)
	v_cndmask_b32_e64 v238, v244, v245, s[50:51]
	ds_bpermute_b32 v244, v243, v71
	ds_bpermute_b32 v245, v243, v73
	s_waitcnt lgkmcnt(0)
	v_cndmask_b32_e64 v239, v244, v245, s[50:51]
	v_mov_b32_e32 v42, v208
	v_mov_b32_e32 v43, v209
	v_mov_b32_e32 v44, v210
	v_mov_b32_e32 v45, v211
	v_mov_b32_e32 v46, v212
	v_mov_b32_e32 v47, v213
	v_mov_b32_e32 v48, v214
	v_mov_b32_e32 v49, v215
	v_mov_b32_e32 v50, v216
	v_mov_b32_e32 v51, v217
	v_mov_b32_e32 v52, v218
	v_mov_b32_e32 v53, v219
	v_mov_b32_e32 v54, v220
	v_mov_b32_e32 v55, v221
	v_mov_b32_e32 v56, v222
	v_mov_b32_e32 v57, v223
	v_mov_b32_e32 v58, v224
	v_mov_b32_e32 v59, v225
	v_mov_b32_e32 v60, v226
	v_mov_b32_e32 v61, v227
	v_mov_b32_e32 v62, v228
	v_mov_b32_e32 v63, v229
	v_mov_b32_e32 v64, v230
	v_mov_b32_e32 v65, v231
	v_mov_b32_e32 v66, v232
	v_mov_b32_e32 v67, v233
	v_mov_b32_e32 v68, v234
	v_mov_b32_e32 v69, v235
	v_mov_b32_e32 v70, v236
	v_mov_b32_e32 v71, v237
	v_mov_b32_e32 v72, v238
	v_mov_b32_e32 v73, v239
	ds_bpermute_b32 v244, v242, v74
	ds_bpermute_b32 v245, v242, v76
	s_waitcnt lgkmcnt(0)
	v_cndmask_b32_e64 v208, v244, v245, s[50:51]
	ds_bpermute_b32 v244, v242, v90
	ds_bpermute_b32 v245, v242, v92
	s_waitcnt lgkmcnt(0)
	v_cndmask_b32_e64 v209, v244, v245, s[50:51]
	ds_bpermute_b32 v244, v242, v75
	ds_bpermute_b32 v245, v242, v77
	s_waitcnt lgkmcnt(0)
	v_cndmask_b32_e64 v210, v244, v245, s[50:51]
	ds_bpermute_b32 v244, v242, v91
	ds_bpermute_b32 v245, v242, v93
	s_waitcnt lgkmcnt(0)
	v_cndmask_b32_e64 v211, v244, v245, s[50:51]
	ds_bpermute_b32 v244, v243, v74
	ds_bpermute_b32 v245, v243, v76
	s_waitcnt lgkmcnt(0)
	v_cndmask_b32_e64 v212, v244, v245, s[50:51]
	ds_bpermute_b32 v244, v243, v90
	ds_bpermute_b32 v245, v243, v92
	s_waitcnt lgkmcnt(0)
	v_cndmask_b32_e64 v213, v244, v245, s[50:51]
	ds_bpermute_b32 v244, v243, v75
	ds_bpermute_b32 v245, v243, v77
	s_waitcnt lgkmcnt(0)
	v_cndmask_b32_e64 v214, v244, v245, s[50:51]
	ds_bpermute_b32 v244, v243, v91
	ds_bpermute_b32 v245, v243, v93
	s_waitcnt lgkmcnt(0)
	v_cndmask_b32_e64 v215, v244, v245, s[50:51]
	ds_bpermute_b32 v244, v242, v78
	ds_bpermute_b32 v245, v242, v80
	s_waitcnt lgkmcnt(0)
	v_cndmask_b32_e64 v216, v244, v245, s[50:51]
	ds_bpermute_b32 v244, v242, v94
	ds_bpermute_b32 v245, v242, v96
	s_waitcnt lgkmcnt(0)
	v_cndmask_b32_e64 v217, v244, v245, s[50:51]
	ds_bpermute_b32 v244, v242, v79
	ds_bpermute_b32 v245, v242, v81
	s_waitcnt lgkmcnt(0)
	v_cndmask_b32_e64 v218, v244, v245, s[50:51]
	ds_bpermute_b32 v244, v242, v95
	ds_bpermute_b32 v245, v242, v97
	s_waitcnt lgkmcnt(0)
	v_cndmask_b32_e64 v219, v244, v245, s[50:51]
	ds_bpermute_b32 v244, v243, v78
	ds_bpermute_b32 v245, v243, v80
	s_waitcnt lgkmcnt(0)
	v_cndmask_b32_e64 v220, v244, v245, s[50:51]
	ds_bpermute_b32 v244, v243, v94
	ds_bpermute_b32 v245, v243, v96
	s_waitcnt lgkmcnt(0)
	v_cndmask_b32_e64 v221, v244, v245, s[50:51]
	ds_bpermute_b32 v244, v243, v79
	ds_bpermute_b32 v245, v243, v81
	s_waitcnt lgkmcnt(0)
	v_cndmask_b32_e64 v222, v244, v245, s[50:51]
	ds_bpermute_b32 v244, v243, v95
	ds_bpermute_b32 v245, v243, v97
	s_waitcnt lgkmcnt(0)
	v_cndmask_b32_e64 v223, v244, v245, s[50:51]
	ds_bpermute_b32 v244, v242, v82
	ds_bpermute_b32 v245, v242, v84
	s_waitcnt lgkmcnt(0)
	v_cndmask_b32_e64 v224, v244, v245, s[50:51]
	ds_bpermute_b32 v244, v242, v98
	ds_bpermute_b32 v245, v242, v100
	s_waitcnt lgkmcnt(0)
	v_cndmask_b32_e64 v225, v244, v245, s[50:51]
	ds_bpermute_b32 v244, v242, v83
	ds_bpermute_b32 v245, v242, v85
	s_waitcnt lgkmcnt(0)
	v_cndmask_b32_e64 v226, v244, v245, s[50:51]
	ds_bpermute_b32 v244, v242, v99
	ds_bpermute_b32 v245, v242, v101
	s_waitcnt lgkmcnt(0)
	v_cndmask_b32_e64 v227, v244, v245, s[50:51]
	ds_bpermute_b32 v244, v243, v82
	ds_bpermute_b32 v245, v243, v84
	s_waitcnt lgkmcnt(0)
	v_cndmask_b32_e64 v228, v244, v245, s[50:51]
	ds_bpermute_b32 v244, v243, v98
	ds_bpermute_b32 v245, v243, v100
	s_waitcnt lgkmcnt(0)
	v_cndmask_b32_e64 v229, v244, v245, s[50:51]
	ds_bpermute_b32 v244, v243, v83
	ds_bpermute_b32 v245, v243, v85
	s_waitcnt lgkmcnt(0)
	v_cndmask_b32_e64 v230, v244, v245, s[50:51]
	ds_bpermute_b32 v244, v243, v99
	ds_bpermute_b32 v245, v243, v101
	s_waitcnt lgkmcnt(0)
	v_cndmask_b32_e64 v231, v244, v245, s[50:51]
	ds_bpermute_b32 v244, v242, v86
	ds_bpermute_b32 v245, v242, v88
	s_waitcnt lgkmcnt(0)
	v_cndmask_b32_e64 v232, v244, v245, s[50:51]
	ds_bpermute_b32 v244, v242, v102
	ds_bpermute_b32 v245, v242, v104
	s_waitcnt lgkmcnt(0)
	v_cndmask_b32_e64 v233, v244, v245, s[50:51]
	ds_bpermute_b32 v244, v242, v87
	ds_bpermute_b32 v245, v242, v89
	s_waitcnt lgkmcnt(0)
	v_cndmask_b32_e64 v234, v244, v245, s[50:51]
	ds_bpermute_b32 v244, v242, v103
	ds_bpermute_b32 v245, v242, v105
	s_waitcnt lgkmcnt(0)
	v_cndmask_b32_e64 v235, v244, v245, s[50:51]
	ds_bpermute_b32 v244, v243, v86
	ds_bpermute_b32 v245, v243, v88
	s_waitcnt lgkmcnt(0)
	v_cndmask_b32_e64 v236, v244, v245, s[50:51]
	ds_bpermute_b32 v244, v243, v102
	ds_bpermute_b32 v245, v243, v104
	s_waitcnt lgkmcnt(0)
	v_cndmask_b32_e64 v237, v244, v245, s[50:51]
	ds_bpermute_b32 v244, v243, v87
	ds_bpermute_b32 v245, v243, v89
	s_waitcnt lgkmcnt(0)
	v_cndmask_b32_e64 v238, v244, v245, s[50:51]
	ds_bpermute_b32 v244, v243, v103
	ds_bpermute_b32 v245, v243, v105
	s_waitcnt lgkmcnt(0)
	v_cndmask_b32_e64 v239, v244, v245, s[50:51]
	v_mov_b32_e32 v74, v208
	v_mov_b32_e32 v75, v209
	v_mov_b32_e32 v76, v210
	v_mov_b32_e32 v77, v211
	v_mov_b32_e32 v78, v212
	v_mov_b32_e32 v79, v213
	v_mov_b32_e32 v80, v214
	v_mov_b32_e32 v81, v215
	v_mov_b32_e32 v82, v216
	v_mov_b32_e32 v83, v217
	v_mov_b32_e32 v84, v218
	v_mov_b32_e32 v85, v219
	v_mov_b32_e32 v86, v220
	v_mov_b32_e32 v87, v221
	v_mov_b32_e32 v88, v222
	v_mov_b32_e32 v89, v223
	v_mov_b32_e32 v90, v224
	v_mov_b32_e32 v91, v225
	v_mov_b32_e32 v92, v226
	v_mov_b32_e32 v93, v227
	v_mov_b32_e32 v94, v228
	v_mov_b32_e32 v95, v229
	v_mov_b32_e32 v96, v230
	v_mov_b32_e32 v97, v231
	v_mov_b32_e32 v98, v232
	v_mov_b32_e32 v99, v233
	v_mov_b32_e32 v100, v234
	v_mov_b32_e32 v101, v235
	v_mov_b32_e32 v102, v236
	v_mov_b32_e32 v103, v237
	v_mov_b32_e32 v104, v238
	v_mov_b32_e32 v105, v239
	ds_bpermute_b32 v244, v242, v2
	ds_bpermute_b32 v245, v242, v4
	s_waitcnt lgkmcnt(0)
	v_cndmask_b32_e64 v248, v244, v245, s[50:51]
	ds_bpermute_b32 v244, v242, v22
	ds_bpermute_b32 v245, v242, v24
	s_waitcnt lgkmcnt(0)
	v_cndmask_b32_e64 v249, v244, v245, s[50:51]
	ds_bpermute_b32 v244, v242, v3
	ds_bpermute_b32 v245, v242, v5
	s_waitcnt lgkmcnt(0)
	v_cndmask_b32_e64 v250, v244, v245, s[50:51]
	ds_bpermute_b32 v244, v242, v23
	ds_bpermute_b32 v245, v242, v25
	s_waitcnt lgkmcnt(0)
	v_cndmask_b32_e64 v251, v244, v245, s[50:51]
	ds_bpermute_b32 v244, v243, v2
	ds_bpermute_b32 v245, v243, v4
	s_waitcnt lgkmcnt(0)
	v_cndmask_b32_e64 v252, v244, v245, s[50:51]
	ds_bpermute_b32 v244, v243, v22
	ds_bpermute_b32 v245, v243, v24
	s_waitcnt lgkmcnt(0)
	v_cndmask_b32_e64 v253, v244, v245, s[50:51]
	ds_bpermute_b32 v244, v243, v3
	ds_bpermute_b32 v245, v243, v5
	s_waitcnt lgkmcnt(0)
	v_cndmask_b32_e64 v254, v244, v245, s[50:51]
	ds_bpermute_b32 v244, v243, v23
	ds_bpermute_b32 v245, v243, v25
	s_waitcnt lgkmcnt(0)
	v_cndmask_b32_e64 v255, v244, v245, s[50:51]
	v_mov_b32_e32 v131, v134
	v_lshrrev_b32_e32 v186, 6, v0
	s_nop 0
	v_readfirstlane_b32 s46, v186
	s_cmp_lt_u32 s46, 2
	s_cbranch_scc1 .Lskip_prio
	s_setprio 1
.Lskip_prio:
	.p2align 6
